# baseline (speedup 1.0000x reference)
.LBB0_6:
	s_load_dwordx4 s[12:15], s[0:1], 0x10
	s_load_dwordx2 s[16:17], s[0:1], 0x20
	v_and_b32_e32 v33, 15, v0
	v_bfe_u32 v32, v0, 4, 2
	v_mov_b32_e32 v1, 0
	v_accvgpr_write_b32 a0, 0
	v_accvgpr_write_b32 a1, 0
	v_accvgpr_write_b32 a2, 0
	v_accvgpr_write_b32 a3, 0
	v_accvgpr_write_b32 a4, 0
	v_accvgpr_write_b32 a5, 0
	v_accvgpr_write_b32 a6, 0
	v_accvgpr_write_b32 a7, 0
	v_accvgpr_write_b32 a8, 0
	v_accvgpr_write_b32 a9, 0
	v_accvgpr_write_b32 a10, 0
	v_accvgpr_write_b32 a11, 0
	v_accvgpr_write_b32 a12, 0
	v_accvgpr_write_b32 a13, 0
	v_accvgpr_write_b32 a14, 0
	s_andn2_b64 vcc, exec, s[18:19]
	v_accvgpr_write_b32 a15, 0
	s_cbranch_vccnz .LBB0_16
	v_lshrrev_b32_e32 v44, 4, v0
	v_and_b32_e32 v36, 0x78, v4
	v_or_b32_e32 v4, s20, v44
	v_min_i32_e32 v0, s25, v4
	v_mad_i64_i32 v[2:3], s[0:1], v0, s10, 0
	v_or_b32_e32 v5, s22, v44
	s_waitcnt lgkmcnt(0)
	v_lshl_add_u64 v[2:3], v[2:3], 1, s[4:5]
	v_lshlrev_b32_e32 v0, 1, v36
	v_lshl_add_u64 v[16:17], v[2:3], 0, v[0:1]
	v_min_i32_e32 v2, s24, v5
	v_mad_i64_i32 v[2:3], s[0:1], v2, s10, 0
	v_lshl_add_u64 v[2:3], v[2:3], 1, s[6:7]
	v_lshl_add_u64 v[18:19], v[2:3], 0, v[0:1]
	v_add_u32_e32 v2, 16, v4
	v_min_i32_e32 v2, s25, v2
	v_mad_i64_i32 v[2:3], s[0:1], v2, s10, 0
	v_lshl_add_u64 v[2:3], v[2:3], 1, s[4:5]
	v_lshl_add_u64 v[20:21], v[2:3], 0, v[0:1]
	v_add_u32_e32 v2, 16, v5
	v_min_i32_e32 v2, s24, v2
	v_mad_i64_i32 v[2:3], s[0:1], v2, s10, 0
	v_lshl_add_u64 v[2:3], v[2:3], 1, s[6:7]
	v_lshl_add_u64 v[22:23], v[2:3], 0, v[0:1]
	v_add_u32_e32 v2, 32, v4
	v_min_i32_e32 v2, s25, v2
	v_mad_i64_i32 v[2:3], s[0:1], v2, s10, 0
	v_lshl_add_u64 v[2:3], v[2:3], 1, s[4:5]
	v_lshl_add_u64 v[24:25], v[2:3], 0, v[0:1]
	v_add_u32_e32 v2, 32, v5
	v_min_i32_e32 v2, s24, v2
	v_mad_i64_i32 v[2:3], s[0:1], v2, s10, 0
	v_lshl_add_u64 v[2:3], v[2:3], 1, s[6:7]
	v_lshl_add_u64 v[26:27], v[2:3], 0, v[0:1]
	v_add_u32_e32 v2, 48, v4
	v_min_i32_e32 v2, s25, v2
	v_mad_i64_i32 v[2:3], s[0:1], v2, s10, 0
	v_lshl_add_u64 v[2:3], v[2:3], 1, s[4:5]
	v_lshl_add_u64 v[28:29], v[2:3], 0, v[0:1]
	v_add_u32_e32 v2, 48, v5
	v_min_i32_e32 v2, s24, v2
	v_mad_i64_i32 v[2:3], s[0:1], v2, s10, 0
	v_add_u32_e32 v37, s26, v36
	s_add_i32 s18, s11, -8
	v_lshl_add_u64 v[2:3], v[2:3], 1, s[6:7]
	v_lshl_add_u64 v[30:31], v[2:3], 0, v[0:1]
	v_min_i32_e32 v0, s18, v37
	v_sub_u32_e32 v0, v0, v36
	v_ashrrev_i32_e32 v1, 31, v0
	v_lshlrev_b64 v[8:9], 1, v[0:1]
	v_lshl_add_u64 v[0:1], v[18:19], 0, v[8:9]
	v_lshl_add_u64 v[2:3], v[22:23], 0, v[8:9]
	global_load_dwordx4 v[54:57], v[0:1], off
	global_load_dwordx4 v[58:61], v[2:3], off
	v_lshl_add_u64 v[0:1], v[26:27], 0, v[8:9]
	v_lshl_add_u64 v[2:3], v[30:31], 0, v[8:9]
	v_lshl_add_u64 v[10:11], v[16:17], 0, v[8:9]
	v_lshl_add_u64 v[12:13], v[20:21], 0, v[8:9]
	v_lshl_add_u64 v[40:41], v[24:25], 0, v[8:9]
	global_load_dwordx4 v[62:65], v[0:1], off
	global_load_dwordx4 v[66:69], v[2:3], off
	s_nop 0
	global_load_dwordx4 v[0:3], v[10:11], off
	global_load_dwordx4 v[4:7], v[12:13], off
	v_lshl_add_u64 v[42:43], v[28:29], 0, v[8:9]
	global_load_dwordx4 v[8:11], v[40:41], off
	global_load_dwordx4 v[12:15], v[42:43], off
	v_accvgpr_write_b32 a0, 0
	v_mul_u32_u24_e32 v38, 0xa8, v38
	v_or_b32_e32 v43, v34, v33
	v_mul_u32_u24_e32 v40, 0xa8, v44
	v_accvgpr_mov_b32 a3, a0
	v_add_lshl_u32 v38, v38, v39, 1
	s_movk_i32 s4, 0x5400
	v_or_b32_e32 v42, v35, v33
	v_add_lshl_u32 v40, v40, v36, 1
	s_movk_i32 s5, 0x150
	v_mul_u32_u24_e32 v43, 0x150, v43
	v_lshlrev_b32_e32 v44, 4, v32
	v_accvgpr_mov_b32 a1, a0
	v_accvgpr_mov_b32 a2, a0
	v_accvgpr_mov_b32 a7, a3
	v_accvgpr_mov_b32 a11, a3
	v_accvgpr_mov_b32 a15, a3
	v_cmp_gt_i32_e64 s[0:1], s11, v37
	s_add_i32 s6, s23, -1
	v_add_u32_e32 v39, 0x5400, v38
	v_add_u32_e32 v41, 0x5400, v40
	v_mad_u32_u24 v42, v42, s5, v44
	v_add3_u32 v43, v43, v44, s4
	s_mov_b32 s7, 0
	v_accvgpr_mov_b32 a6, a2
	v_accvgpr_mov_b32 a5, a1
	v_accvgpr_mov_b32 a4, a0
	v_accvgpr_mov_b32 a10, a2
	v_accvgpr_mov_b32 a9, a1
	v_accvgpr_mov_b32 a8, a0
	v_accvgpr_mov_b32 a14, a2
	v_accvgpr_mov_b32 a13, a1
	v_accvgpr_mov_b32 a12, a0
	v_min_i32_e32 v44, s18, v37
	v_sub_u32_e32 v44, v44, v36
	v_ashrrev_i32_e32 v45, 31, v44
	v_lshlrev_b64 v[44:45], 1, v[44:45]
	v_lshl_add_u64 v[18:19], v[18:19], 0, v[44:45]
	v_lshl_add_u64 v[22:23], v[22:23], 0, v[44:45]
	v_lshl_add_u64 v[26:27], v[26:27], 0, v[44:45]
	v_lshl_add_u64 v[30:31], v[30:31], 0, v[44:45]
	v_lshl_add_u64 v[16:17], v[16:17], 0, v[44:45]
	v_lshl_add_u64 v[20:21], v[20:21], 0, v[44:45]
	v_lshl_add_u64 v[24:25], v[24:25], 0, v[44:45]
	v_lshl_add_u64 v[28:29], v[28:29], 0, v[44:45]
	global_load_dwordx4 v[104:107], v[18:19], off offset:256
	global_load_dwordx4 v[108:111], v[22:23], off offset:256
	global_load_dwordx4 v[112:115], v[26:27], off offset:256
	global_load_dwordx4 v[116:119], v[30:31], off offset:256
	global_load_dwordx4 v[88:91], v[16:17], off offset:256
	global_load_dwordx4 v[92:95], v[20:21], off offset:256
	global_load_dwordx4 v[96:99], v[24:25], off offset:256
	global_load_dwordx4 v[100:103], v[28:29], off offset:256
	s_waitcnt vmcnt(14)
	ds_write_b128 v41, v[54:57]
	ds_write_b128 v41, v[58:61] offset:5376
	s_waitcnt vmcnt(12)
	ds_write_b128 v41, v[62:65] offset:10752
	ds_write_b128 v41, v[66:69] offset:16128
	s_waitcnt vmcnt(10)
	ds_write_b128 v40, v[0:3]
	ds_write_b128 v40, v[4:7] offset:5376
	s_waitcnt vmcnt(8)
	ds_write_b128 v40, v[8:11] offset:10752
	ds_write_b128 v40, v[12:15] offset:16128
	s_waitcnt lgkmcnt(0)
	global_load_dwordx4 v[54:57], v[18:19], off offset:512
	global_load_dwordx4 v[58:61], v[22:23], off offset:512
	global_load_dwordx4 v[62:65], v[26:27], off offset:512
	global_load_dwordx4 v[66:69], v[30:31], off offset:512
	global_load_dwordx4 v[0:3], v[16:17], off offset:512
	global_load_dwordx4 v[4:7], v[20:21], off offset:512
	global_load_dwordx4 v[8:11], v[24:25], off offset:512
	global_load_dwordx4 v[12:15], v[28:29], off offset:512
	s_barrier
	ds_read_b128 v[70:73], v42
	ds_read_b128 v[74:77], v43
	ds_read_b128 v[78:81], v42 offset:5376
	ds_read_b128 v[82:85], v43 offset:5376
	ds_read_b128 v[120:123], v42 offset:64
	ds_read_b128 v[124:127], v43 offset:64
	ds_read_b128 v[128:131], v42 offset:5440
	ds_read_b128 v[132:135], v43 offset:5440
	s_waitcnt lgkmcnt(6)
	v_mfma_f32_16x16x32_f16 a[12:15], v[70:73], v[74:77], a[12:15]
	s_waitcnt lgkmcnt(4)
	v_mfma_f32_16x16x32_f16 a[8:11], v[70:73], v[82:85], a[8:11]
	v_mfma_f32_16x16x32_f16 a[4:7], v[78:81], v[74:77], a[4:7]
	v_mfma_f32_16x16x32_f16 a[0:3], v[78:81], v[82:85], a[0:3]
	ds_read_b128 v[70:73], v42 offset:128
	ds_read_b128 v[74:77], v43 offset:128
	ds_read_b128 v[78:81], v42 offset:5504
	ds_read_b128 v[82:85], v43 offset:5504
	s_waitcnt lgkmcnt(6)
	v_mfma_f32_16x16x32_f16 a[12:15], v[120:123], v[124:127], a[12:15]
	s_waitcnt lgkmcnt(4)
	v_mfma_f32_16x16x32_f16 a[8:11], v[120:123], v[132:135], a[8:11]
	v_mfma_f32_16x16x32_f16 a[4:7], v[128:131], v[124:127], a[4:7]
	v_mfma_f32_16x16x32_f16 a[0:3], v[128:131], v[132:135], a[0:3]
	ds_read_b128 v[120:123], v42 offset:192
	ds_read_b128 v[124:127], v43 offset:192
	ds_read_b128 v[128:131], v42 offset:5568
	ds_read_b128 v[132:135], v43 offset:5568
	s_waitcnt lgkmcnt(6)
	v_mfma_f32_16x16x32_f16 a[12:15], v[70:73], v[74:77], a[12:15]
	s_waitcnt lgkmcnt(4)
	v_mfma_f32_16x16x32_f16 a[8:11], v[70:73], v[82:85], a[8:11]
	v_mfma_f32_16x16x32_f16 a[4:7], v[78:81], v[74:77], a[4:7]
	v_mfma_f32_16x16x32_f16 a[0:3], v[78:81], v[82:85], a[0:3]
	s_waitcnt lgkmcnt(2)
	v_mfma_f32_16x16x32_f16 a[12:15], v[120:123], v[124:127], a[12:15]
	s_waitcnt lgkmcnt(0)
	v_mfma_f32_16x16x32_f16 a[8:11], v[120:123], v[132:135], a[8:11]
	v_mfma_f32_16x16x32_f16 a[4:7], v[128:131], v[124:127], a[4:7]
	v_mfma_f32_16x16x32_f16 a[0:3], v[128:131], v[132:135], a[0:3]
	s_barrier
	s_waitcnt vmcnt(14)
	ds_write_b128 v41, v[104:107]
	ds_write_b128 v41, v[108:111] offset:5376
	s_waitcnt vmcnt(12)
	ds_write_b128 v41, v[112:115] offset:10752
	ds_write_b128 v41, v[116:119] offset:16128
	s_waitcnt vmcnt(10)
	ds_write_b128 v40, v[88:91]
	ds_write_b128 v40, v[92:95] offset:5376
	s_waitcnt vmcnt(8)
	ds_write_b128 v40, v[96:99] offset:10752
	ds_write_b128 v40, v[100:103] offset:16128
	s_waitcnt lgkmcnt(0)
	global_load_dwordx4 v[104:107], v[18:19], off offset:768
	global_load_dwordx4 v[108:111], v[22:23], off offset:768
	global_load_dwordx4 v[112:115], v[26:27], off offset:768
	global_load_dwordx4 v[116:119], v[30:31], off offset:768
	global_load_dwordx4 v[88:91], v[16:17], off offset:768
	global_load_dwordx4 v[92:95], v[20:21], off offset:768
	global_load_dwordx4 v[96:99], v[24:25], off offset:768
	global_load_dwordx4 v[100:103], v[28:29], off offset:768
	s_barrier
	ds_read_b128 v[70:73], v42
	ds_read_b128 v[74:77], v43
	ds_read_b128 v[78:81], v42 offset:5376
	ds_read_b128 v[82:85], v43 offset:5376
	ds_read_b128 v[120:123], v42 offset:64
	ds_read_b128 v[124:127], v43 offset:64
	ds_read_b128 v[128:131], v42 offset:5440
	ds_read_b128 v[132:135], v43 offset:5440
	s_waitcnt lgkmcnt(6)
	v_mfma_f32_16x16x32_f16 a[12:15], v[70:73], v[74:77], a[12:15]
	s_waitcnt lgkmcnt(4)
	v_mfma_f32_16x16x32_f16 a[8:11], v[70:73], v[82:85], a[8:11]
	v_mfma_f32_16x16x32_f16 a[4:7], v[78:81], v[74:77], a[4:7]
	v_mfma_f32_16x16x32_f16 a[0:3], v[78:81], v[82:85], a[0:3]
	ds_read_b128 v[70:73], v42 offset:128
	ds_read_b128 v[74:77], v43 offset:128
	ds_read_b128 v[78:81], v42 offset:5504
	ds_read_b128 v[82:85], v43 offset:5504
	s_waitcnt lgkmcnt(6)
	v_mfma_f32_16x16x32_f16 a[12:15], v[120:123], v[124:127], a[12:15]
	s_waitcnt lgkmcnt(4)
	v_mfma_f32_16x16x32_f16 a[8:11], v[120:123], v[132:135], a[8:11]
	v_mfma_f32_16x16x32_f16 a[4:7], v[128:131], v[124:127], a[4:7]
	v_mfma_f32_16x16x32_f16 a[0:3], v[128:131], v[132:135], a[0:3]
	ds_read_b128 v[120:123], v42 offset:192
	ds_read_b128 v[124:127], v43 offset:192
	ds_read_b128 v[128:131], v42 offset:5568
	ds_read_b128 v[132:135], v43 offset:5568
	s_waitcnt lgkmcnt(6)
	v_mfma_f32_16x16x32_f16 a[12:15], v[70:73], v[74:77], a[12:15]
	s_waitcnt lgkmcnt(4)
	v_mfma_f32_16x16x32_f16 a[8:11], v[70:73], v[82:85], a[8:11]
	v_mfma_f32_16x16x32_f16 a[4:7], v[78:81], v[74:77], a[4:7]
	v_mfma_f32_16x16x32_f16 a[0:3], v[78:81], v[82:85], a[0:3]
	s_waitcnt lgkmcnt(2)
	v_mfma_f32_16x16x32_f16 a[12:15], v[120:123], v[124:127], a[12:15]
	s_waitcnt lgkmcnt(0)
	v_mfma_f32_16x16x32_f16 a[8:11], v[120:123], v[132:135], a[8:11]
	v_mfma_f32_16x16x32_f16 a[4:7], v[128:131], v[124:127], a[4:7]
	v_mfma_f32_16x16x32_f16 a[0:3], v[128:131], v[132:135], a[0:3]
	s_barrier
	s_waitcnt vmcnt(14)
	ds_write_b128 v41, v[54:57]
	ds_write_b128 v41, v[58:61] offset:5376
	s_waitcnt vmcnt(12)
	ds_write_b128 v41, v[62:65] offset:10752
	ds_write_b128 v41, v[66:69] offset:16128
	s_waitcnt vmcnt(10)
	ds_write_b128 v40, v[0:3]
	ds_write_b128 v40, v[4:7] offset:5376
	s_waitcnt vmcnt(8)
	ds_write_b128 v40, v[8:11] offset:10752
	ds_write_b128 v40, v[12:15] offset:16128
	s_waitcnt lgkmcnt(0)
	global_load_dwordx4 v[54:57], v[18:19], off offset:1024
	global_load_dwordx4 v[58:61], v[22:23], off offset:1024
	global_load_dwordx4 v[62:65], v[26:27], off offset:1024
	global_load_dwordx4 v[66:69], v[30:31], off offset:1024
	global_load_dwordx4 v[0:3], v[16:17], off offset:1024
	global_load_dwordx4 v[4:7], v[20:21], off offset:1024
	global_load_dwordx4 v[8:11], v[24:25], off offset:1024
	global_load_dwordx4 v[12:15], v[28:29], off offset:1024
	s_barrier
	ds_read_b128 v[70:73], v42
	ds_read_b128 v[74:77], v43
	ds_read_b128 v[78:81], v42 offset:5376
	ds_read_b128 v[82:85], v43 offset:5376
	ds_read_b128 v[120:123], v42 offset:64
	ds_read_b128 v[124:127], v43 offset:64
	ds_read_b128 v[128:131], v42 offset:5440
	ds_read_b128 v[132:135], v43 offset:5440
	s_waitcnt lgkmcnt(6)
	v_mfma_f32_16x16x32_f16 a[12:15], v[70:73], v[74:77], a[12:15]
	s_waitcnt lgkmcnt(4)
	v_mfma_f32_16x16x32_f16 a[8:11], v[70:73], v[82:85], a[8:11]
	v_mfma_f32_16x16x32_f16 a[4:7], v[78:81], v[74:77], a[4:7]
	v_mfma_f32_16x16x32_f16 a[0:3], v[78:81], v[82:85], a[0:3]
	ds_read_b128 v[70:73], v42 offset:128
	ds_read_b128 v[74:77], v43 offset:128
	ds_read_b128 v[78:81], v42 offset:5504
	ds_read_b128 v[82:85], v43 offset:5504
	s_waitcnt lgkmcnt(6)
	v_mfma_f32_16x16x32_f16 a[12:15], v[120:123], v[124:127], a[12:15]
	s_waitcnt lgkmcnt(4)
	v_mfma_f32_16x16x32_f16 a[8:11], v[120:123], v[132:135], a[8:11]
	v_mfma_f32_16x16x32_f16 a[4:7], v[128:131], v[124:127], a[4:7]
	v_mfma_f32_16x16x32_f16 a[0:3], v[128:131], v[132:135], a[0:3]
	ds_read_b128 v[120:123], v42 offset:192
	ds_read_b128 v[124:127], v43 offset:192
	ds_read_b128 v[128:131], v42 offset:5568
	ds_read_b128 v[132:135], v43 offset:5568
	s_waitcnt lgkmcnt(6)
	v_mfma_f32_16x16x32_f16 a[12:15], v[70:73], v[74:77], a[12:15]
	s_waitcnt lgkmcnt(4)
	v_mfma_f32_16x16x32_f16 a[8:11], v[70:73], v[82:85], a[8:11]
	v_mfma_f32_16x16x32_f16 a[4:7], v[78:81], v[74:77], a[4:7]
	v_mfma_f32_16x16x32_f16 a[0:3], v[78:81], v[82:85], a[0:3]
	s_waitcnt lgkmcnt(2)
	v_mfma_f32_16x16x32_f16 a[12:15], v[120:123], v[124:127], a[12:15]
	s_waitcnt lgkmcnt(0)
	v_mfma_f32_16x16x32_f16 a[8:11], v[120:123], v[132:135], a[8:11]
	v_mfma_f32_16x16x32_f16 a[4:7], v[128:131], v[124:127], a[4:7]
	v_mfma_f32_16x16x32_f16 a[0:3], v[128:131], v[132:135], a[0:3]
	s_barrier
	s_waitcnt vmcnt(14)
	ds_write_b128 v41, v[104:107]
	ds_write_b128 v41, v[108:111] offset:5376
	s_waitcnt vmcnt(12)
	ds_write_b128 v41, v[112:115] offset:10752
	ds_write_b128 v41, v[116:119] offset:16128
	s_waitcnt vmcnt(10)
	ds_write_b128 v40, v[88:91]
	ds_write_b128 v40, v[92:95] offset:5376
	s_waitcnt vmcnt(8)
	ds_write_b128 v40, v[96:99] offset:10752
	ds_write_b128 v40, v[100:103] offset:16128
	s_waitcnt lgkmcnt(0)
	global_load_dwordx4 v[104:107], v[18:19], off offset:1280
	global_load_dwordx4 v[108:111], v[22:23], off offset:1280
	global_load_dwordx4 v[112:115], v[26:27], off offset:1280
	global_load_dwordx4 v[116:119], v[30:31], off offset:1280
	global_load_dwordx4 v[88:91], v[16:17], off offset:1280
	global_load_dwordx4 v[92:95], v[20:21], off offset:1280
	global_load_dwordx4 v[96:99], v[24:25], off offset:1280
	global_load_dwordx4 v[100:103], v[28:29], off offset:1280
	s_barrier
	ds_read_b128 v[70:73], v42
	ds_read_b128 v[74:77], v43
	ds_read_b128 v[78:81], v42 offset:5376
	ds_read_b128 v[82:85], v43 offset:5376
	ds_read_b128 v[120:123], v42 offset:64
	ds_read_b128 v[124:127], v43 offset:64
	ds_read_b128 v[128:131], v42 offset:5440
	ds_read_b128 v[132:135], v43 offset:5440
	s_waitcnt lgkmcnt(6)
	v_mfma_f32_16x16x32_f16 a[12:15], v[70:73], v[74:77], a[12:15]
	s_waitcnt lgkmcnt(4)
	v_mfma_f32_16x16x32_f16 a[8:11], v[70:73], v[82:85], a[8:11]
	v_mfma_f32_16x16x32_f16 a[4:7], v[78:81], v[74:77], a[4:7]
	v_mfma_f32_16x16x32_f16 a[0:3], v[78:81], v[82:85], a[0:3]
	ds_read_b128 v[70:73], v42 offset:128
	ds_read_b128 v[74:77], v43 offset:128
	ds_read_b128 v[78:81], v42 offset:5504
	ds_read_b128 v[82:85], v43 offset:5504
	s_waitcnt lgkmcnt(6)
	v_mfma_f32_16x16x32_f16 a[12:15], v[120:123], v[124:127], a[12:15]
	s_waitcnt lgkmcnt(4)
	v_mfma_f32_16x16x32_f16 a[8:11], v[120:123], v[132:135], a[8:11]
	v_mfma_f32_16x16x32_f16 a[4:7], v[128:131], v[124:127], a[4:7]
	v_mfma_f32_16x16x32_f16 a[0:3], v[128:131], v[132:135], a[0:3]
	ds_read_b128 v[120:123], v42 offset:192
	ds_read_b128 v[124:127], v43 offset:192
	ds_read_b128 v[128:131], v42 offset:5568
	ds_read_b128 v[132:135], v43 offset:5568
	s_waitcnt lgkmcnt(6)
	v_mfma_f32_16x16x32_f16 a[12:15], v[70:73], v[74:77], a[12:15]
	s_waitcnt lgkmcnt(4)
	v_mfma_f32_16x16x32_f16 a[8:11], v[70:73], v[82:85], a[8:11]
	v_mfma_f32_16x16x32_f16 a[4:7], v[78:81], v[74:77], a[4:7]
	v_mfma_f32_16x16x32_f16 a[0:3], v[78:81], v[82:85], a[0:3]
	s_waitcnt lgkmcnt(2)
	v_mfma_f32_16x16x32_f16 a[12:15], v[120:123], v[124:127], a[12:15]
	s_waitcnt lgkmcnt(0)
	v_mfma_f32_16x16x32_f16 a[8:11], v[120:123], v[132:135], a[8:11]
	v_mfma_f32_16x16x32_f16 a[4:7], v[128:131], v[124:127], a[4:7]
	v_mfma_f32_16x16x32_f16 a[0:3], v[128:131], v[132:135], a[0:3]
	s_barrier
	s_waitcnt vmcnt(14)
	ds_write_b128 v41, v[54:57]
	ds_write_b128 v41, v[58:61] offset:5376
	s_waitcnt vmcnt(12)
	ds_write_b128 v41, v[62:65] offset:10752
	ds_write_b128 v41, v[66:69] offset:16128
	s_waitcnt vmcnt(10)
	ds_write_b128 v40, v[0:3]
	ds_write_b128 v40, v[4:7] offset:5376
	s_waitcnt vmcnt(8)
	ds_write_b128 v40, v[8:11] offset:10752
	ds_write_b128 v40, v[12:15] offset:16128
	s_waitcnt lgkmcnt(0)
	global_load_dwordx4 v[54:57], v[18:19], off offset:1536
	global_load_dwordx4 v[58:61], v[22:23], off offset:1536
	global_load_dwordx4 v[62:65], v[26:27], off offset:1536
	global_load_dwordx4 v[66:69], v[30:31], off offset:1536
	global_load_dwordx4 v[0:3], v[16:17], off offset:1536
	global_load_dwordx4 v[4:7], v[20:21], off offset:1536
	global_load_dwordx4 v[8:11], v[24:25], off offset:1536
	global_load_dwordx4 v[12:15], v[28:29], off offset:1536
	s_barrier
	ds_read_b128 v[70:73], v42
	ds_read_b128 v[74:77], v43
	ds_read_b128 v[78:81], v42 offset:5376
	ds_read_b128 v[82:85], v43 offset:5376
	ds_read_b128 v[120:123], v42 offset:64
	ds_read_b128 v[124:127], v43 offset:64
	ds_read_b128 v[128:131], v42 offset:5440
	ds_read_b128 v[132:135], v43 offset:5440
	s_waitcnt lgkmcnt(6)
	v_mfma_f32_16x16x32_f16 a[12:15], v[70:73], v[74:77], a[12:15]
	s_waitcnt lgkmcnt(4)
	v_mfma_f32_16x16x32_f16 a[8:11], v[70:73], v[82:85], a[8:11]
	v_mfma_f32_16x16x32_f16 a[4:7], v[78:81], v[74:77], a[4:7]
	v_mfma_f32_16x16x32_f16 a[0:3], v[78:81], v[82:85], a[0:3]
	ds_read_b128 v[70:73], v42 offset:128
	ds_read_b128 v[74:77], v43 offset:128
	ds_read_b128 v[78:81], v42 offset:5504
	ds_read_b128 v[82:85], v43 offset:5504
	s_waitcnt lgkmcnt(6)
	v_mfma_f32_16x16x32_f16 a[12:15], v[120:123], v[124:127], a[12:15]
	s_waitcnt lgkmcnt(4)
	v_mfma_f32_16x16x32_f16 a[8:11], v[120:123], v[132:135], a[8:11]
	v_mfma_f32_16x16x32_f16 a[4:7], v[128:131], v[124:127], a[4:7]
	v_mfma_f32_16x16x32_f16 a[0:3], v[128:131], v[132:135], a[0:3]
	ds_read_b128 v[120:123], v42 offset:192
	ds_read_b128 v[124:127], v43 offset:192
	ds_read_b128 v[128:131], v42 offset:5568
	ds_read_b128 v[132:135], v43 offset:5568
	s_waitcnt lgkmcnt(6)
	v_mfma_f32_16x16x32_f16 a[12:15], v[70:73], v[74:77], a[12:15]
	s_waitcnt lgkmcnt(4)
	v_mfma_f32_16x16x32_f16 a[8:11], v[70:73], v[82:85], a[8:11]
	v_mfma_f32_16x16x32_f16 a[4:7], v[78:81], v[74:77], a[4:7]
	v_mfma_f32_16x16x32_f16 a[0:3], v[78:81], v[82:85], a[0:3]
	s_waitcnt lgkmcnt(2)
	v_mfma_f32_16x16x32_f16 a[12:15], v[120:123], v[124:127], a[12:15]
	s_waitcnt lgkmcnt(0)
	v_mfma_f32_16x16x32_f16 a[8:11], v[120:123], v[132:135], a[8:11]
	v_mfma_f32_16x16x32_f16 a[4:7], v[128:131], v[124:127], a[4:7]
	v_mfma_f32_16x16x32_f16 a[0:3], v[128:131], v[132:135], a[0:3]
	s_barrier
	s_waitcnt vmcnt(14)
	ds_write_b128 v41, v[104:107]
	ds_write_b128 v41, v[108:111] offset:5376
	s_waitcnt vmcnt(12)
	ds_write_b128 v41, v[112:115] offset:10752
	ds_write_b128 v41, v[116:119] offset:16128
	s_waitcnt vmcnt(10)
	ds_write_b128 v40, v[88:91]
	ds_write_b128 v40, v[92:95] offset:5376
	s_waitcnt vmcnt(8)
	ds_write_b128 v40, v[96:99] offset:10752
	ds_write_b128 v40, v[100:103] offset:16128
	s_waitcnt lgkmcnt(0)
	s_barrier
	ds_read_b128 v[70:73], v42
	ds_read_b128 v[74:77], v43
	ds_read_b128 v[78:81], v42 offset:5376
	ds_read_b128 v[82:85], v43 offset:5376
	ds_read_b128 v[120:123], v42 offset:64
	ds_read_b128 v[124:127], v43 offset:64
	ds_read_b128 v[128:131], v42 offset:5440
	ds_read_b128 v[132:135], v43 offset:5440
	s_waitcnt lgkmcnt(6)
	v_mfma_f32_16x16x32_f16 a[12:15], v[70:73], v[74:77], a[12:15]
	s_waitcnt lgkmcnt(4)
	v_mfma_f32_16x16x32_f16 a[8:11], v[70:73], v[82:85], a[8:11]
	v_mfma_f32_16x16x32_f16 a[4:7], v[78:81], v[74:77], a[4:7]
	v_mfma_f32_16x16x32_f16 a[0:3], v[78:81], v[82:85], a[0:3]
	ds_read_b128 v[70:73], v42 offset:128
	ds_read_b128 v[74:77], v43 offset:128
	ds_read_b128 v[78:81], v42 offset:5504
	ds_read_b128 v[82:85], v43 offset:5504
	s_waitcnt lgkmcnt(6)
	v_mfma_f32_16x16x32_f16 a[12:15], v[120:123], v[124:127], a[12:15]
	s_waitcnt lgkmcnt(4)
	v_mfma_f32_16x16x32_f16 a[8:11], v[120:123], v[132:135], a[8:11]
	v_mfma_f32_16x16x32_f16 a[4:7], v[128:131], v[124:127], a[4:7]
	v_mfma_f32_16x16x32_f16 a[0:3], v[128:131], v[132:135], a[0:3]
	ds_read_b128 v[120:123], v42 offset:192
	ds_read_b128 v[124:127], v43 offset:192
	ds_read_b128 v[128:131], v42 offset:5568
	ds_read_b128 v[132:135], v43 offset:5568
	s_waitcnt lgkmcnt(6)
	v_mfma_f32_16x16x32_f16 a[12:15], v[70:73], v[74:77], a[12:15]
	s_waitcnt lgkmcnt(4)
	v_mfma_f32_16x16x32_f16 a[8:11], v[70:73], v[82:85], a[8:11]
	v_mfma_f32_16x16x32_f16 a[4:7], v[78:81], v[74:77], a[4:7]
	v_mfma_f32_16x16x32_f16 a[0:3], v[78:81], v[82:85], a[0:3]
	s_waitcnt lgkmcnt(2)
	v_mfma_f32_16x16x32_f16 a[12:15], v[120:123], v[124:127], a[12:15]
	s_waitcnt lgkmcnt(0)
	v_mfma_f32_16x16x32_f16 a[8:11], v[120:123], v[132:135], a[8:11]
	v_mfma_f32_16x16x32_f16 a[4:7], v[128:131], v[124:127], a[4:7]
	v_mfma_f32_16x16x32_f16 a[0:3], v[128:131], v[132:135], a[0:3]
	s_barrier
	s_waitcnt vmcnt(6)
	ds_write_b128 v41, v[54:57]
	ds_write_b128 v41, v[58:61] offset:5376
	s_waitcnt vmcnt(4)
	ds_write_b128 v41, v[62:65] offset:10752
	ds_write_b128 v41, v[66:69] offset:16128
	s_waitcnt vmcnt(2)
	ds_write_b128 v40, v[0:3]
	ds_write_b128 v40, v[4:7] offset:5376
	s_waitcnt vmcnt(0)
	ds_write_b128 v40, v[8:11] offset:10752
	ds_write_b128 v40, v[12:15] offset:16128
	ds_write_b128 v38, v[46:49] offset:256
	ds_write_b128 v39, v[50:53] offset:256
	s_waitcnt lgkmcnt(0)
	s_barrier
	ds_read_b128 v[70:73], v42
	ds_read_b128 v[74:77], v43
	ds_read_b128 v[78:81], v42 offset:5376
	ds_read_b128 v[82:85], v43 offset:5376
	ds_read_b128 v[120:123], v42 offset:64
	ds_read_b128 v[124:127], v43 offset:64
	ds_read_b128 v[128:131], v42 offset:5440
	ds_read_b128 v[132:135], v43 offset:5440
	s_waitcnt lgkmcnt(6)
	v_mfma_f32_16x16x32_f16 a[12:15], v[70:73], v[74:77], a[12:15]
	s_waitcnt lgkmcnt(4)
	v_mfma_f32_16x16x32_f16 a[8:11], v[70:73], v[82:85], a[8:11]
	v_mfma_f32_16x16x32_f16 a[4:7], v[78:81], v[74:77], a[4:7]
	v_mfma_f32_16x16x32_f16 a[0:3], v[78:81], v[82:85], a[0:3]
	ds_read_b128 v[70:73], v42 offset:128
	ds_read_b128 v[74:77], v43 offset:128
	ds_read_b128 v[78:81], v42 offset:5504
	ds_read_b128 v[82:85], v43 offset:5504
	s_waitcnt lgkmcnt(6)
	v_mfma_f32_16x16x32_f16 a[12:15], v[120:123], v[124:127], a[12:15]
	s_waitcnt lgkmcnt(4)
	v_mfma_f32_16x16x32_f16 a[8:11], v[120:123], v[132:135], a[8:11]
	v_mfma_f32_16x16x32_f16 a[4:7], v[128:131], v[124:127], a[4:7]
	v_mfma_f32_16x16x32_f16 a[0:3], v[128:131], v[132:135], a[0:3]
	ds_read_b128 v[120:123], v42 offset:192
	ds_read_b128 v[124:127], v43 offset:192
	ds_read_b128 v[128:131], v42 offset:5568
	ds_read_b128 v[132:135], v43 offset:5568
	s_waitcnt lgkmcnt(6)
	v_mfma_f32_16x16x32_f16 a[12:15], v[70:73], v[74:77], a[12:15]
	s_waitcnt lgkmcnt(4)
	v_mfma_f32_16x16x32_f16 a[8:11], v[70:73], v[82:85], a[8:11]
	v_mfma_f32_16x16x32_f16 a[4:7], v[78:81], v[74:77], a[4:7]
	v_mfma_f32_16x16x32_f16 a[0:3], v[78:81], v[82:85], a[0:3]
	ds_read_b128 v[70:73], v42 offset:256
	ds_read_b128 v[74:77], v43 offset:256
	ds_read_b128 v[78:81], v42 offset:5632
	ds_read_b128 v[82:85], v43 offset:5632
	s_waitcnt lgkmcnt(6)
	v_mfma_f32_16x16x32_f16 a[12:15], v[120:123], v[124:127], a[12:15]
	s_waitcnt lgkmcnt(4)
	v_mfma_f32_16x16x32_f16 a[8:11], v[120:123], v[132:135], a[8:11]
	v_mfma_f32_16x16x32_f16 a[4:7], v[128:131], v[124:127], a[4:7]
	v_mfma_f32_16x16x32_f16 a[0:3], v[128:131], v[132:135], a[0:3]
	s_waitcnt lgkmcnt(2)
	v_mfma_f32_16x16x32_f16 a[12:15], v[70:73], v[74:77], a[12:15]
	s_waitcnt lgkmcnt(0)
	v_mfma_f32_16x16x32_f16 a[8:11], v[70:73], v[82:85], a[8:11]
	v_mfma_f32_16x16x32_f16 a[4:7], v[78:81], v[74:77], a[4:7]
	v_mfma_f32_16x16x32_f16 a[0:3], v[78:81], v[82:85], a[0:3]
	s_barrier
	s_waitcnt vmcnt(4)
	v_mov_b32_e32 v3, v34
	v_mov_b32_e32 v2, v35

.LBB4_82:
	s_barrier
	ds_read_b128 v[108:111], v105
	ds_read_b128 v[112:115], v106
	ds_read_b128 v[116:119], v105 offset:4352
	ds_read_b128 v[120:123], v106 offset:4352
	s_andn2_b64 s[4:5], s[4:5], exec
	s_and_b64 s[20:21], s[0:1], exec
	s_waitcnt lgkmcnt(2)
	v_mfma_f32_16x16x32_f16 a[0:3], v[108:111], v[112:115], a[0:3]
	s_or_b64 s[4:5], s[4:5], s[20:21]
	v_add_u32_e32 v104, 0x80, v104
	s_cmp_eq_u32 s14, s13
	s_waitcnt lgkmcnt(0)
	v_mfma_f32_16x16x32_f16 a[4:7], v[108:111], v[120:123], a[4:7]
	v_mfma_f32_16x16x32_f16 a[8:11], v[116:119], v[112:115], a[8:11]
	v_mfma_f32_16x16x32_f16 a[12:15], v[116:119], v[120:123], a[12:15]
	ds_read_b128 v[108:111], v105 offset:64
	ds_read_b128 v[112:115], v106 offset:64
	ds_read_b128 v[116:119], v105 offset:4416
	ds_read_b128 v[120:123], v106 offset:4416
	s_waitcnt lgkmcnt(2)
	v_mfma_f32_16x16x32_f16 a[0:3], v[108:111], v[112:115], a[0:3]
	s_waitcnt lgkmcnt(0)
	v_mfma_f32_16x16x32_f16 a[4:7], v[108:111], v[120:123], a[4:7]
	v_mfma_f32_16x16x32_f16 a[8:11], v[116:119], v[112:115], a[8:11]
	v_mfma_f32_16x16x32_f16 a[12:15], v[116:119], v[120:123], a[12:15]
	ds_read_b128 v[108:111], v105 offset:128
	ds_read_b128 v[112:115], v106 offset:128
	ds_read_b128 v[116:119], v105 offset:4480
	ds_read_b128 v[120:123], v106 offset:4480
	s_waitcnt lgkmcnt(2)
	v_mfma_f32_16x16x32_f16 a[0:3], v[108:111], v[112:115], a[0:3]
	s_waitcnt lgkmcnt(0)
	v_mfma_f32_16x16x32_f16 a[4:7], v[108:111], v[120:123], a[4:7]
	v_mfma_f32_16x16x32_f16 a[8:11], v[116:119], v[112:115], a[8:11]
	v_mfma_f32_16x16x32_f16 a[12:15], v[116:119], v[120:123], a[12:15]
	ds_read_b128 v[108:111], v105 offset:192
	ds_read_b128 v[112:115], v106 offset:192
	ds_read_b128 v[116:119], v105 offset:4544
	ds_read_b128 v[120:123], v106 offset:4544
	s_waitcnt lgkmcnt(0)
	s_barrier
	v_mfma_f32_16x16x32_f16 a[0:3], v[108:111], v[112:115], a[0:3]
	v_mfma_f32_16x16x32_f16 a[4:7], v[108:111], v[120:123], a[4:7]
	v_mfma_f32_16x16x32_f16 a[8:11], v[116:119], v[112:115], a[8:11]
	v_mfma_f32_16x16x32_f16 a[12:15], v[116:119], v[120:123], a[12:15]
	s_cbranch_scc1 .LBB4_85
.LBB4_83:
	s_waitcnt vmcnt(0)
	v_cvt_pk_f16_f32 v107, v2, v3
	v_cvt_pk_f16_f32 v108, v4, v5
	v_cndmask_b32_e64 v109, 0, v108, s[4:5]
	v_cndmask_b32_e64 v108, 0, v107, s[4:5]
	ds_write_b64 v102, v[108:109]
	v_cvt_pk_f16_f32 v109, v8, v9
	v_cvt_pk_f16_f32 v108, v6, v7
	ds_write_b64 v103, v[108:109]
	v_cvt_pk_f16_f32 v107, v10, v11
	v_cvt_pk_f16_f32 v108, v12, v13
	v_cndmask_b32_e64 v109, 0, v108, s[4:5]
	v_cndmask_b32_e64 v108, 0, v107, s[4:5]
	ds_write_b64 v102, v[108:109] offset:2176
	v_cvt_pk_f16_f32 v109, v16, v17
	v_cvt_pk_f16_f32 v108, v14, v15
	ds_write_b64 v103, v[108:109] offset:2176
	v_cvt_pk_f16_f32 v107, v18, v19
	v_cvt_pk_f16_f32 v108, v20, v21
	v_cndmask_b32_e64 v109, 0, v108, s[4:5]
	v_cndmask_b32_e64 v108, 0, v107, s[4:5]
	ds_write_b64 v102, v[108:109] offset:4352
	v_cvt_pk_f16_f32 v109, v24, v25
	v_cvt_pk_f16_f32 v108, v22, v23
	ds_write_b64 v103, v[108:109] offset:4352
	v_cvt_pk_f16_f32 v107, v26, v27
	v_cvt_pk_f16_f32 v108, v28, v29
	v_cndmask_b32_e64 v109, 0, v108, s[4:5]
	v_cndmask_b32_e64 v108, 0, v107, s[4:5]
	ds_write_b64 v102, v[108:109] offset:6528
	v_cvt_pk_f16_f32 v109, v32, v33
	v_cvt_pk_f16_f32 v108, v30, v31
	ds_write_b64 v103, v[108:109] offset:6528
	v_cvt_pk_f16_f32 v107, v34, v35
	v_cvt_pk_f16_f32 v108, v36, v37
	v_cndmask_b32_e64 v109, 0, v108, s[4:5]
	v_cndmask_b32_e64 v108, 0, v107, s[4:5]
	ds_write_b64 v102, v[108:109] offset:8704
	v_cvt_pk_f16_f32 v109, v40, v41
	v_cvt_pk_f16_f32 v108, v38, v39
	ds_write_b64 v103, v[108:109] offset:8704
	v_cvt_pk_f16_f32 v107, v42, v43
	v_cvt_pk_f16_f32 v108, v44, v45
	v_cndmask_b32_e64 v109, 0, v108, s[4:5]
	v_cndmask_b32_e64 v108, 0, v107, s[4:5]
	ds_write_b64 v102, v[108:109] offset:10880
	v_cvt_pk_f16_f32 v109, v48, v49
	v_cvt_pk_f16_f32 v108, v46, v47
	ds_write_b64 v103, v[108:109] offset:10880
	v_cvt_pk_f16_f32 v107, v50, v51
	v_cvt_pk_f16_f32 v108, v52, v53
	v_cndmask_b32_e64 v109, 0, v108, s[4:5]
	v_cndmask_b32_e64 v108, 0, v107, s[4:5]
	ds_write_b64 v102, v[108:109] offset:13056
	v_cvt_pk_f16_f32 v109, v56, v57
	v_cvt_pk_f16_f32 v108, v54, v55
	ds_write_b64 v103, v[108:109] offset:13056
	v_cvt_pk_f16_f32 v107, v58, v59
	v_cvt_pk_f16_f32 v108, v60, v61
	s_andn2_b64 s[0:1], s[0:1], exec
	s_and_b64 s[20:21], s[4:5], exec
	v_cndmask_b32_e64 v109, 0, v108, s[4:5]
	v_cndmask_b32_e64 v108, 0, v107, s[4:5]
	s_add_i32 s13, s13, 1
	s_or_b64 s[0:1], s[0:1], s[20:21]
	ds_write_b64 v102, v[108:109] offset:15232
	v_cvt_pk_f16_f32 v109, v64, v65
	v_cvt_pk_f16_f32 v108, v62, v63
	s_cmp_lt_i32 s13, s14
	ds_write_b64 v103, v[108:109] offset:15232
	s_waitcnt lgkmcnt(0)
	s_cbranch_scc0 .LBB4_82
	v_min_i32_e32 v2, s10, v104
	v_sub_u32_e32 v2, v2, v66
	v_ashrrev_i32_e32 v3, 31, v2
	v_lshlrev_b64 v[62:63], 2, v[2:3]
	v_lshl_add_u64 v[2:3], v[96:97], 0, v[62:63]
	v_lshl_add_u64 v[6:7], v[98:99], 0, v[62:63]
	v_lshl_add_u64 v[10:11], v[92:93], 0, v[62:63]
	v_lshl_add_u64 v[14:15], v[94:95], 0, v[62:63]
	v_lshl_add_u64 v[18:19], v[88:89], 0, v[62:63]
	v_lshl_add_u64 v[22:23], v[90:91], 0, v[62:63]
	v_lshl_add_u64 v[26:27], v[84:85], 0, v[62:63]
	v_lshl_add_u64 v[30:31], v[86:87], 0, v[62:63]
	v_lshl_add_u64 v[34:35], v[80:81], 0, v[62:63]
	v_lshl_add_u64 v[38:39], v[82:83], 0, v[62:63]
	v_lshl_add_u64 v[42:43], v[76:77], 0, v[62:63]
	v_lshl_add_u64 v[46:47], v[78:79], 0, v[62:63]
	v_lshl_add_u64 v[50:51], v[72:73], 0, v[62:63]
	v_lshl_add_u64 v[54:55], v[74:75], 0, v[62:63]
	v_lshl_add_u64 v[58:59], v[68:69], 0, v[62:63]
	v_lshl_add_u64 v[62:63], v[70:71], 0, v[62:63]
	global_load_dwordx4 v[2:5], v[2:3], off
	v_cmp_gt_i32_e32 vcc, s12, v104
	global_load_dwordx4 v[6:9], v[6:7], off
	s_andn2_b64 s[0:1], s[0:1], exec
	global_load_dwordx4 v[10:13], v[10:11], off
	s_and_b64 s[4:5], vcc, exec
	global_load_dwordx4 v[14:17], v[14:15], off
	s_or_b64 s[0:1], s[0:1], s[4:5]
	global_load_dwordx4 v[18:21], v[18:19], off
	s_nop 0
	global_load_dwordx4 v[22:25], v[22:23], off
	s_nop 0
	global_load_dwordx4 v[26:29], v[26:27], off
	s_nop 0
	global_load_dwordx4 v[30:33], v[30:31], off
	s_nop 0
	global_load_dwordx4 v[34:37], v[34:35], off
	s_nop 0
	global_load_dwordx4 v[38:41], v[38:39], off
	s_nop 0
	global_load_dwordx4 v[42:45], v[42:43], off
	s_nop 0
	global_load_dwordx4 v[46:49], v[46:47], off
	s_nop 0
	global_load_dwordx4 v[50:53], v[50:51], off
	s_nop 0
	global_load_dwordx4 v[54:57], v[54:55], off
	s_nop 0
	global_load_dwordx4 v[58:61], v[58:59], off
	s_nop 0
	global_load_dwordx4 v[62:65], v[62:63], off
	s_branch .LBB4_82
